# baseline (speedup 1.0000x reference)
_Z7gemm_dbILi256ELi192ELi64ELi96ELi64ELi2ELi1ELi4EEvPKDF16_S1_PfPDF16_S3_S3_PK15HIP_vector_typeIfLj2EEiii:
	s_load_dwordx4 s[4:7], s[0:1], 0x38
	s_waitcnt lgkmcnt(0)
	s_and_b32 s7, s2, 7
	s_lshr_b32 s2, s2, 3
	v_readfirstlane_b32 s14, v0
	s_mul_hi_i32 s3, s5, 0x2aaaaaab
	s_lshr_b32 s5, s3, 31
	s_ashr_i32 s3, s3, 5
	s_add_i32 s3, s3, s5
	s_abs_i32 s5, s3
	v_cvt_f32_u32_e32 v1, s5
	s_ashr_i32 s8, s4, 31
	s_lshr_b32 s8, s8, 21
	s_add_i32 s4, s4, s8
	v_rcp_iflag_f32_e32 v1, v1
	s_ashr_i32 s4, s4, 11
	s_mul_i32 s4, s4, s7
	s_sub_i32 s7, 0, s5
	v_mul_f32_e32 v1, 0x4f7ffffe, v1
	v_cvt_u32_f32_e32 v1, v1
	s_ashr_i32 s8, s3, 31
	v_readfirstlane_b32 s9, v1
	s_mul_i32 s7, s7, s9
	s_mul_hi_u32 s7, s9, s7
	s_add_i32 s9, s9, s7
	s_mul_hi_u32 s7, s2, s9
	s_mul_i32 s9, s7, s5
	s_sub_i32 s9, s2, s9
	s_add_i32 s10, s7, 1
	s_sub_i32 s11, s9, s5
	s_cmp_ge_u32 s9, s5
	s_cselect_b32 s7, s10, s7
	s_cselect_b32 s9, s11, s9
	s_add_i32 s10, s7, 1
	s_cmp_ge_u32 s9, s5
	s_cselect_b32 s5, s10, s7
	s_xor_b32 s5, s5, s8
	s_sub_i32 s5, s5, s8
	s_add_i32 s4, s5, s4
	s_mul_i32 s5, s5, s3
	s_sub_i32 s15, s2, s5
	s_ashr_i32 s2, s6, 31
	s_lshr_b32 s2, s2, 26
	s_add_i32 s2, s6, s2
	s_lshl_b32 s12, s4, 8
	s_ashr_i32 s7, s2, 6
	s_cmpk_lt_u32 s14, 0x200
	s_cselect_b64 s[2:3], -1, 0
	s_mul_i32 s13, s15, 0xc0
	s_mov_b64 s[4:5], -1
	s_and_b64 vcc, exec, s[2:3]
	s_cbranch_vccnz .LBB2_9
	v_add_u32_e32 v1, 0xfffffe00, v0
	s_load_dwordx4 s[8:11], s[0:1], 0x0
	v_lshlrev_b32_e32 v18, 4, v1
	v_ashrrev_i32_e32 v19, 3, v1
	v_lshrrev_b32_e32 v1, 4, v1
	v_xor_b32_e32 v1, v1, v0
	v_lshlrev_b32_e32 v1, 4, v1
	v_and_b32_e32 v28, 0x70, v1
	v_add_u32_e32 v1, 0, v18
	v_add_u32_e32 v4, 0x1000, v18
	v_add_u32_e32 v6, 0x2000, v18
	v_add_u32_e32 v8, 0x3000, v18
	v_add_u32_e32 v10, 0x4000, v18
	v_add_u32_e32 v12, 0x5000, v18
	v_add_u32_e32 v14, 0x6000, v18
	v_add_u32_e32 v18, 0x7000, v18
	v_ashrrev_i32_e32 v20, 7, v4
	v_lshrrev_b32_e32 v22, 7, v6
	v_lshrrev_b32_e32 v24, 7, v8
	v_lshrrev_b32_e32 v26, 7, v10
	v_lshrrev_b32_e32 v36, 7, v12
	v_lshrrev_b32_e32 v14, 7, v14
	v_lshrrev_b32_e32 v18, 7, v18
	v_add_u32_e32 v2, s12, v19
	s_movk_i32 s16, 0x880
	s_waitcnt lgkmcnt(0)
	s_mov_b64 s[22:23], s[8:9]
	s_mov_b64 s[24:25], s[10:11]
	v_mov_b64_e32 v[16:17], s[8:9]
	v_add_u32_e32 v4, s12, v20
	v_add_u32_e32 v6, s12, v22
	v_add_u32_e32 v8, s12, v24
	v_add_u32_e32 v10, s12, v26
	v_add_u32_e32 v12, s12, v36
	v_add_u32_e32 v14, s12, v14
	v_add_u32_e32 v18, s12, v18
	v_mad_i64_i32 v[2:3], s[4:5], v2, s16, v[16:17]
	v_mad_i64_i32 v[4:5], s[4:5], v4, s16, v[16:17]
	v_mad_i64_i32 v[6:7], s[4:5], v6, s16, v[16:17]
	v_mad_i64_i32 v[8:9], s[4:5], v8, s16, v[16:17]
	v_mad_i64_i32 v[10:11], s[4:5], v10, s16, v[16:17]
	v_mad_i64_i32 v[12:13], s[4:5], v12, s16, v[16:17]
	v_mad_i64_i32 v[14:15], s[4:5], v14, s16, v[16:17]
	v_mad_i64_i32 v[16:17], s[4:5], v18, s16, v[16:17]
	v_add_u32_e32 v18, s13, v19
	v_mov_b64_e32 v[30:31], s[10:11]
	v_add_u32_e32 v20, s13, v20
	v_add_u32_e32 v22, s13, v22
	v_add_u32_e32 v24, s13, v24
	v_add_u32_e32 v26, s13, v26
	v_add_u32_e32 v36, s13, v36
	v_mad_i64_i32 v[18:19], s[4:5], v18, s16, v[30:31]
	v_mad_i64_i32 v[20:21], s[4:5], v20, s16, v[30:31]
	v_mad_u64_u32 v[22:23], s[4:5], v22, s16, v[30:31]
	v_mad_u64_u32 v[24:25], s[4:5], v24, s16, v[30:31]
	v_mad_u64_u32 v[26:27], s[4:5], v26, s16, v[30:31]
	v_mad_u64_u32 v[30:31], s[4:5], v36, s16, v[30:31]
	v_mov_b32_e32 v29, 0
	v_add_u32_e32 v32, 0x1000, v1
	v_readfirstlane_b32 s4, v1
	v_lshl_add_u64 v[2:3], v[2:3], 0, v[28:29]
	v_add_u32_e32 v33, 0x2000, v1
	s_mov_b32 m0, s4
	v_readfirstlane_b32 s4, v32
	v_lshl_add_u64 v[4:5], v[4:5], 0, v[28:29]
	v_add_u32_e32 v34, 0x3000, v1
	global_load_lds_dwordx4 v[2:3], off
	s_mov_b32 m0, s4
	v_readfirstlane_b32 s4, v33
	v_lshl_add_u64 v[6:7], v[6:7], 0, v[28:29]
	v_add_u32_e32 v35, 0x4000, v1
	global_load_lds_dwordx4 v[4:5], off
	s_mov_b32 m0, s4
	v_readfirstlane_b32 s4, v34
	v_lshl_add_u64 v[8:9], v[8:9], 0, v[28:29]
	v_add_u32_e32 v37, 0x5000, v1
	global_load_lds_dwordx4 v[6:7], off
	s_mov_b32 m0, s4
	v_readfirstlane_b32 s4, v35
	v_lshl_add_u64 v[10:11], v[10:11], 0, v[28:29]
	v_add_u32_e32 v38, 0x6000, v1
	global_load_lds_dwordx4 v[8:9], off
	s_mov_b32 m0, s4
	v_readfirstlane_b32 s4, v37
	v_lshl_add_u64 v[12:13], v[12:13], 0, v[28:29]
	v_add_u32_e32 v39, 0x7000, v1
	global_load_lds_dwordx4 v[10:11], off
	s_mov_b32 m0, s4
	v_readfirstlane_b32 s4, v38
	v_lshl_add_u64 v[14:15], v[14:15], 0, v[28:29]
	v_add_u32_e32 v40, 0x18000, v1
	global_load_lds_dwordx4 v[12:13], off
	s_mov_b32 m0, s4
	v_readfirstlane_b32 s4, v39
	v_lshl_add_u64 v[16:17], v[16:17], 0, v[28:29]
	v_add_u32_e32 v41, 0x19000, v1
	global_load_lds_dwordx4 v[14:15], off
	s_mov_b32 m0, s4
	v_readfirstlane_b32 s4, v40
	v_lshl_add_u64 v[18:19], v[18:19], 0, v[28:29]
	v_add_u32_e32 v42, 0x1a000, v1
	global_load_lds_dwordx4 v[16:17], off
	s_mov_b32 m0, s4
	v_readfirstlane_b32 s4, v41
	v_lshl_add_u64 v[20:21], v[20:21], 0, v[28:29]
	v_add_u32_e32 v43, 0x1b000, v1
	global_load_lds_dwordx4 v[18:19], off
	s_mov_b32 m0, s4
	v_readfirstlane_b32 s4, v42
	v_lshl_add_u64 v[22:23], v[22:23], 0, v[28:29]
	v_add_u32_e32 v44, 0x1c000, v1
	global_load_lds_dwordx4 v[20:21], off
	s_mov_b32 m0, s4
	v_readfirstlane_b32 s4, v43
	v_lshl_add_u64 v[24:25], v[24:25], 0, v[28:29]
	v_lshl_add_u64 v[26:27], v[26:27], 0, v[28:29]
	v_lshl_add_u64 v[28:29], v[30:31], 0, v[28:29]
	v_add_u32_e32 v30, 0x1d000, v1
	global_load_lds_dwordx4 v[22:23], off
	s_mov_b32 m0, s4
	v_readfirstlane_b32 s4, v44
	global_load_lds_dwordx4 v[24:25], off
	s_mov_b32 m0, s4
	v_readfirstlane_b32 s4, v30
	global_load_lds_dwordx4 v[26:27], off
	s_mov_b32 m0, s4
	s_cmp_lt_i32 s6, 64
	global_load_lds_dwordx4 v[28:29], off
	v_readfirstlane_b32 s18, v1
	v_subrev_u32_e32 v2, s22, v2
	v_subrev_u32_e32 v4, s22, v4
	v_subrev_u32_e32 v6, s22, v6
	v_subrev_u32_e32 v8, s22, v8
	v_subrev_u32_e32 v10, s22, v10
	v_subrev_u32_e32 v12, s22, v12
	v_subrev_u32_e32 v14, s22, v14
	v_subrev_u32_e32 v16, s22, v16
	v_subrev_u32_e32 v18, s24, v18
	v_subrev_u32_e32 v20, s24, v20
	v_subrev_u32_e32 v22, s24, v22
	v_subrev_u32_e32 v24, s24, v24
	v_subrev_u32_e32 v26, s24, v26
	v_subrev_u32_e32 v28, s24, v28
	s_add_u32 s26, s22, 0x80
	s_addc_u32 s27, s23, 0
	s_add_i32 s17, s18, 0x8000
	s_mov_b32 m0, s17
	s_add_i32 s17, s17, 0x1000
	global_load_lds_dwordx4 v2, s[26:27]
	s_mov_b32 m0, s17
	s_add_i32 s17, s17, 0x1000
	global_load_lds_dwordx4 v4, s[26:27]
	s_mov_b32 m0, s17
	s_add_i32 s17, s17, 0x1000
	global_load_lds_dwordx4 v6, s[26:27]
	s_mov_b32 m0, s17
	s_add_i32 s17, s17, 0x1000
	global_load_lds_dwordx4 v8, s[26:27]
	s_mov_b32 m0, s17
	s_add_i32 s17, s17, 0x1000
	global_load_lds_dwordx4 v10, s[26:27]
	s_mov_b32 m0, s17
	s_add_i32 s17, s17, 0x1000
	global_load_lds_dwordx4 v12, s[26:27]
	s_mov_b32 m0, s17
	s_add_i32 s17, s17, 0x1000
	global_load_lds_dwordx4 v14, s[26:27]
	s_mov_b32 m0, s17
	s_add_i32 s17, s17, 0x1000
	global_load_lds_dwordx4 v16, s[26:27]
	s_waitcnt vmcnt(8)
	s_barrier
	s_mov_b32 s11, 0
	s_mov_b32 s19, 0x10000
.Lq_ld_loop:
	s_add_i32 s16, s11, 1
	s_cmp_ge_i32 s16, s7
	s_cbranch_scc1 .Lq_ld_nomore
	s_lshl_b32 s8, s16, 7
	s_add_u32 s26, s24, s8
	s_addc_u32 s27, s25, 0
	s_and_b32 s17, s16, 1
	s_mul_i32 s17, s17, 0x6000
	s_add_i32 s17, s17, s18
	s_add_i32 s17, s17, 0x18000
	s_mov_b32 m0, s17
	s_add_i32 s17, s17, 0x1000
	global_load_lds_dwordx4 v18, s[26:27]
	s_mov_b32 m0, s17
	s_add_i32 s17, s17, 0x1000
	global_load_lds_dwordx4 v20, s[26:27]
	s_mov_b32 m0, s17
	s_add_i32 s17, s17, 0x1000
	global_load_lds_dwordx4 v22, s[26:27]
	s_mov_b32 m0, s17
	s_add_i32 s17, s17, 0x1000
	global_load_lds_dwordx4 v24, s[26:27]
	s_mov_b32 m0, s17
	s_add_i32 s17, s17, 0x1000
	global_load_lds_dwordx4 v26, s[26:27]
	s_mov_b32 m0, s17
	s_add_i32 s17, s17, 0x1000
	global_load_lds_dwordx4 v28, s[26:27]
	s_add_i32 s16, s11, 2
	s_cmp_ge_i32 s16, s7
	s_cbranch_scc1 .Lq_ld_lastb
	s_lshl_b32 s8, s16, 7
	s_add_u32 s26, s22, s8
	s_addc_u32 s27, s23, 0
	s_add_i32 s17, s19, s18
	s_mov_b32 m0, s17
	s_add_i32 s17, s17, 0x1000
	global_load_lds_dwordx4 v2, s[26:27]
	s_mov_b32 m0, s17
	s_add_i32 s17, s17, 0x1000
	global_load_lds_dwordx4 v4, s[26:27]
	s_mov_b32 m0, s17
	s_add_i32 s17, s17, 0x1000
	global_load_lds_dwordx4 v6, s[26:27]
	s_mov_b32 m0, s17
	s_add_i32 s17, s17, 0x1000
	global_load_lds_dwordx4 v8, s[26:27]
	s_mov_b32 m0, s17
	s_add_i32 s17, s17, 0x1000
	global_load_lds_dwordx4 v10, s[26:27]
	s_mov_b32 m0, s17
	s_add_i32 s17, s17, 0x1000
	global_load_lds_dwordx4 v12, s[26:27]
	s_mov_b32 m0, s17
	s_add_i32 s17, s17, 0x1000
	global_load_lds_dwordx4 v14, s[26:27]
	s_mov_b32 m0, s17
	s_add_i32 s17, s17, 0x1000
	global_load_lds_dwordx4 v16, s[26:27]
	s_add_i32 s19, s19, 0x8000
	s_cmp_lg_u32 s19, 0x18000
	s_cselect_b32 s19, s19, 0
	s_waitcnt vmcnt(8)
	s_barrier
	s_add_i32 s11, s11, 1
	s_branch .Lq_ld_loop

.LBB2_9:
	s_lshr_b32 s8, s14, 7
	v_and_b32_e32 v1, 15, v0
	v_bfe_u32 v98, v0, 4, 2
	s_bfe_u32 s9, s14, 0x10006
	s_and_b64 vcc, exec, s[4:5]
	s_cbranch_vccz .LBB2_13
	s_barrier
	s_cmp_lt_i32 s6, 64
	s_mov_b32 s4, 0
	s_cbranch_scc1 .LBB2_41
	v_lshrrev_b32_e32 v2, 1, v0
	v_bfe_u32 v3, v0, 1, 3
	v_bitop3_b32 v2, v98, v2, 7 bitop3:0x78
	s_mul_i32 s5, s9, 0x60
	v_lshlrev_b32_e32 v99, 4, v2
	v_bitop3_b32 v2, v98, v3, 4 bitop3:0x36
	v_or_b32_e32 v4, s5, v1
	v_lshlrev_b32_e32 v102, 4, v2
	v_mov_b32_e32 v2, 0
	s_lshl_b32 s5, s8, 13
	v_lshlrev_b32_e32 v100, 7, v1
	v_lshlrev_b32_e32 v101, 7, v4
	v_mov_b32_e32 v3, v2
	v_mov_b32_e32 v4, v2
	v_mov_b32_e32 v5, v2
	v_mov_b32_e32 v6, v2
	v_mov_b32_e32 v7, v2
	v_mov_b32_e32 v8, v2
	v_mov_b32_e32 v9, v2
	v_mov_b32_e32 v34, v2
	v_mov_b32_e32 v35, v2
	v_mov_b32_e32 v36, v2
	v_mov_b32_e32 v37, v2
	v_mov_b32_e32 v38, v2
	v_mov_b32_e32 v39, v2
	v_mov_b32_e32 v40, v2
	v_mov_b32_e32 v41, v2
	v_mov_b32_e32 v66, v2
	v_mov_b32_e32 v67, v2
	v_mov_b32_e32 v68, v2
	v_mov_b32_e32 v69, v2
	v_mov_b32_e32 v70, v2
	v_mov_b32_e32 v71, v2
	v_mov_b32_e32 v72, v2
	v_mov_b32_e32 v73, v2
	v_mov_b32_e32 v10, v2
	v_mov_b32_e32 v11, v2
	v_mov_b32_e32 v12, v2
	v_mov_b32_e32 v13, v2
	v_mov_b32_e32 v14, v2
	v_mov_b32_e32 v15, v2
	v_mov_b32_e32 v16, v2
	v_mov_b32_e32 v17, v2
	v_mov_b32_e32 v42, v2
	v_mov_b32_e32 v43, v2
	v_mov_b32_e32 v44, v2
	v_mov_b32_e32 v45, v2
	v_mov_b32_e32 v46, v2
	v_mov_b32_e32 v47, v2
	v_mov_b32_e32 v48, v2
	v_mov_b32_e32 v49, v2
	v_mov_b32_e32 v74, v2
	v_mov_b32_e32 v75, v2
	v_mov_b32_e32 v76, v2
	v_mov_b32_e32 v77, v2
	v_mov_b32_e32 v78, v2
	v_mov_b32_e32 v79, v2
	v_mov_b32_e32 v80, v2
	v_mov_b32_e32 v81, v2
	v_mov_b32_e32 v18, v2
	v_mov_b32_e32 v19, v2
	v_mov_b32_e32 v20, v2
	v_mov_b32_e32 v21, v2
	v_mov_b32_e32 v22, v2
	v_mov_b32_e32 v23, v2
	v_mov_b32_e32 v24, v2
	v_mov_b32_e32 v25, v2
	v_mov_b32_e32 v50, v2
	v_mov_b32_e32 v51, v2
	v_mov_b32_e32 v52, v2
	v_mov_b32_e32 v53, v2
	v_mov_b32_e32 v54, v2
	v_mov_b32_e32 v55, v2
	v_mov_b32_e32 v56, v2
	v_mov_b32_e32 v57, v2
	v_mov_b32_e32 v82, v2
	v_mov_b32_e32 v83, v2
	v_mov_b32_e32 v84, v2
	v_mov_b32_e32 v85, v2
	v_mov_b32_e32 v86, v2
	v_mov_b32_e32 v87, v2
	v_mov_b32_e32 v88, v2
	v_mov_b32_e32 v89, v2
	v_mov_b32_e32 v26, v2
	v_mov_b32_e32 v27, v2
	v_mov_b32_e32 v28, v2
	v_mov_b32_e32 v29, v2
	v_mov_b32_e32 v30, v2
	v_mov_b32_e32 v31, v2
	v_mov_b32_e32 v32, v2
	v_mov_b32_e32 v33, v2
	v_mov_b32_e32 v58, v2
	v_mov_b32_e32 v59, v2
	v_mov_b32_e32 v60, v2
	v_mov_b32_e32 v61, v2
	v_mov_b32_e32 v62, v2
	v_mov_b32_e32 v63, v2
	v_mov_b32_e32 v64, v2
	v_mov_b32_e32 v65, v2
	v_mov_b32_e32 v90, v2
	v_mov_b32_e32 v91, v2
	v_mov_b32_e32 v92, v2
	v_mov_b32_e32 v93, v2
	v_mov_b32_e32 v94, v2
	v_mov_b32_e32 v95, v2
	v_mov_b32_e32 v96, v2
	v_mov_b32_e32 v97, v2
	s_mov_b32 s20, 0
	.p2align	6

	.amdhsa_kernel _Z7gemm_dbILi256ELi192ELi64ELi96ELi64ELi2ELi1ELi4EEvPKDF16_S1_PfPDF16_S3_S3_PK15HIP_vector_typeIfLj2EEiii
		.amdhsa_group_segment_fixed_size 32768
		.amdhsa_private_segment_fixed_size 0
		.amdhsa_kernarg_size 68
		.amdhsa_user_sgpr_count 2
		.amdhsa_user_sgpr_dispatch_ptr 0
		.amdhsa_user_sgpr_queue_ptr 0
		.amdhsa_user_sgpr_kernarg_segment_ptr 1
		.amdhsa_user_sgpr_dispatch_id 0
		.amdhsa_user_sgpr_kernarg_preload_length 0
		.amdhsa_user_sgpr_kernarg_preload_offset 0
		.amdhsa_user_sgpr_private_segment_size 0
		.amdhsa_uses_dynamic_stack 0
		.amdhsa_enable_private_segment 0
		.amdhsa_system_sgpr_workgroup_id_x 1
		.amdhsa_system_sgpr_workgroup_id_y 0
		.amdhsa_system_sgpr_workgroup_id_z 0
		.amdhsa_system_sgpr_workgroup_info 0
		.amdhsa_system_vgpr_workitem_id 0
		.amdhsa_next_free_vgpr 137
		.amdhsa_next_free_sgpr 28
		.amdhsa_accum_offset 140
		.amdhsa_reserve_vcc 1
		.amdhsa_float_round_mode_32 0
		.amdhsa_float_round_mode_16_64 0
		.amdhsa_float_denorm_mode_32 3
		.amdhsa_float_denorm_mode_16_64 3
		.amdhsa_dx10_clamp 1
		.amdhsa_ieee_mode 1
		.amdhsa_fp16_overflow 0
		.amdhsa_tg_split 0
		.amdhsa_exception_fp_ieee_invalid_op 0
		.amdhsa_exception_fp_denorm_src 0
		.amdhsa_exception_fp_ieee_div_zero 0
		.amdhsa_exception_fp_ieee_overflow 0
		.amdhsa_exception_fp_ieee_underflow 0
		.amdhsa_exception_fp_ieee_inexact 0
		.amdhsa_exception_int_div_zero 0
	.end_amdhsa_kernel

amdhsa.kernels:
  - .agpr_count:     0
    .args:
      - .actual_access:  read_only
        .address_space:  global
        .offset:         0
        .size:           8
        .value_kind:     global_buffer
      - .actual_access:  read_only
        .address_space:  global
        .offset:         8
        .size:           8
        .value_kind:     global_buffer
      - .actual_access:  read_only
        .address_space:  global
        .offset:         16
        .size:           8
        .value_kind:     global_buffer
      - .actual_access:  read_only
        .address_space:  global
        .offset:         24
        .size:           8
        .value_kind:     global_buffer
      - .actual_access:  read_only
        .address_space:  global
        .offset:         32
        .size:           8
        .value_kind:     global_buffer
      - .address_space:  global
        .offset:         40
        .size:           8
        .value_kind:     global_buffer
      - .address_space:  global
        .offset:         48
        .size:           8
        .value_kind:     global_buffer
      - .address_space:  global
        .offset:         56
        .size:           8
        .value_kind:     global_buffer
      - .address_space:  global
        .offset:         64
        .size:           8
        .value_kind:     global_buffer
    .group_segment_fixed_size: 0
    .kernarg_segment_align: 8
    .kernarg_segment_size: 72
    .language:       OpenCL C
    .language_version:
      - 2
      - 0
    .max_flat_workgroup_size: 256
    .name:           _Z11prep_kernelPKfS0_S0_S0_S0_PDF16_S1_S1_P15HIP_vector_typeIfLj2EE
    .private_segment_fixed_size: 0
    .sgpr_count:     22
    .sgpr_spill_count: 0
    .symbol:         _Z11prep_kernelPKfS0_S0_S0_S0_PDF16_S1_S1_P15HIP_vector_typeIfLj2EE.kd
    .uniform_work_group_size: 1
    .uses_dynamic_stack: false
    .vgpr_count:     20
    .vgpr_spill_count: 0
    .wavefront_size: 64
  - .agpr_count:     0
    .args:
      - .address_space:  global
        .offset:         0
        .size:           8
        .value_kind:     global_buffer
      - .address_space:  global
        .offset:         8
        .size:           8
        .value_kind:     global_buffer
      - .address_space:  global
        .offset:         16
        .size:           8
        .value_kind:     global_buffer
      - .address_space:  global
        .offset:         24
        .size:           8
        .value_kind:     global_buffer
    .group_segment_fixed_size: 0
    .kernarg_segment_align: 8
    .kernarg_segment_size: 32
    .language:       OpenCL C
    .language_version:
      - 2
      - 0
    .max_flat_workgroup_size: 512
    .name:           _Z10attn64_fwdPKDF16_S0_S0_PDF16_
    .private_segment_fixed_size: 0
    .sgpr_count:     48
    .sgpr_spill_count: 0
    .symbol:         _Z10attn64_fwdPKDF16_S0_S0_PDF16_.kd
    .uniform_work_group_size: 1
    .uses_dynamic_stack: false
    .vgpr_count:     252
    .vgpr_spill_count: 0
    .wavefront_size: 64
  - .agpr_count:     0
    .args:
      - .address_space:  global
        .offset:         0
        .size:           8
        .value_kind:     global_buffer
      - .address_space:  global
        .offset:         8
        .size:           8
        .value_kind:     global_buffer
      - .address_space:  global
        .offset:         16
        .size:           8
        .value_kind:     global_buffer
      - .address_space:  global
        .offset:         24
        .size:           8
        .value_kind:     global_buffer
      - .address_space:  global
        .offset:         32
        .size:           8
        .value_kind:     global_buffer
      - .address_space:  global
        .offset:         40
        .size:           8
        .value_kind:     global_buffer
      - .actual_access:  read_only
        .address_space:  global
        .offset:         48
        .size:           8
        .value_kind:     global_buffer
      - .offset:         56
        .size:           4
        .value_kind:     by_value
      - .offset:         60
        .size:           4
        .value_kind:     by_value
      - .offset:         64
        .size:           4
        .value_kind:     by_value
    .group_segment_fixed_size: 32768
    .kernarg_segment_align: 8
    .kernarg_segment_size: 68
    .language:       OpenCL C
    .language_version:
      - 2
      - 0
    .max_flat_workgroup_size: 768
    .name:           _Z7gemm_dbILi256ELi192ELi64ELi96ELi64ELi2ELi1ELi4EEvPKDF16_S1_PfPDF16_S3_S3_PK15HIP_vector_typeIfLj2EEiii
    .private_segment_fixed_size: 0
    .sgpr_count:     34
    .sgpr_spill_count: 0
    .symbol:         _Z7gemm_dbILi256ELi192ELi64ELi96ELi64ELi2ELi1ELi4EEvPKDF16_S1_PfPDF16_S3_S3_PK15HIP_vector_typeIfLj2EEiii.kd
    .uniform_work_group_size: 1
    .uses_dynamic_stack: false
    .vgpr_count:     137
    .vgpr_spill_count: 0
    .wavefront_size: 64
  - .agpr_count:     0
    .args:
      - .address_space:  global
        .offset:         0
        .size:           8
        .value_kind:     global_buffer
      - .address_space:  global
        .offset:         8
        .size:           8
        .value_kind:     global_buffer
      - .address_space:  global
        .offset:         16
        .size:           8
        .value_kind:     global_buffer
      - .address_space:  global
        .offset:         24
        .size:           8
        .value_kind:     global_buffer
      - .address_space:  global
        .offset:         32
        .size:           8
        .value_kind:     global_buffer
      - .address_space:  global
        .offset:         40
        .size:           8
        .value_kind:     global_buffer
      - .actual_access:  read_only
        .address_space:  global
        .offset:         48
        .size:           8
        .value_kind:     global_buffer
      - .offset:         56
        .size:           4
        .value_kind:     by_value
      - .offset:         60
        .size:           4
        .value_kind:     by_value
      - .offset:         64
        .size:           4
        .value_kind:     by_value
    .group_segment_fixed_size: 0
    .kernarg_segment_align: 8
    .kernarg_segment_size: 68
    .language:       OpenCL C
    .language_version:
      - 2
      - 0
    .max_flat_workgroup_size: 512
    .name:           _Z7gemm_dbILi128ELi128ELi64ELi64ELi64ELi3ELi0ELi4EEvPKDF16_S1_PfPDF16_S3_S3_PK15HIP_vector_typeIfLj2EEiii
    .private_segment_fixed_size: 0
    .sgpr_count:     26
    .sgpr_spill_count: 0
    .symbol:         _Z7gemm_dbILi128ELi128ELi64ELi64ELi64ELi3ELi0ELi4EEvPKDF16_S1_PfPDF16_S3_S3_PK15HIP_vector_typeIfLj2EEiii.kd
    .uniform_work_group_size: 1
    .uses_dynamic_stack: false
    .vgpr_count:     168
    .vgpr_spill_count: 0
    .wavefront_size: 64
